# P1: units of the padded n-tile (pn=15) skip the MFMAs whose accumulators are never stored
# baseline (speedup 1.0000x reference)
; #define PG8_STAGE(bufoff, gbase, voff) do { if constexpr (!(Sched::CRIP & 2)) _Pragma("unroll") for (int _i = 0; _i < 2; ++_i) { unsigned _o = (voff)[_i]; asm volatile("" : "+v"(_o)); \
;         __builtin_amdgcn_global_load_lds((const unsigned*)((const char*)(gbase) + _o), (LAS unsigned*)(lds + (bufoff) + ldsw + _i * 8192), 16, 0, 0); } } while (0)
; #define PG8_LDA(dst, b, h) do { if constexpr (!(Sched::CRIP & 4)) _Pragma("unroll") for (int m = 0; m < 4; ++m) dst[m] = PG8_CAT(*(const LAS i32x4*)(lds + PG8_SA(b, h) + aoff + m * 2048), *(const LAS i32x4*)(lds + PG8_SA(b, h) + aoff + m * 2048 + 1024)); } while (0)
; #define PG8_LDB(dst, b, h) do { if constexpr (!(Sched::CRIP & 4)) _Pragma("unroll") for (int n = 0; n < 2; ++n) dst[n] = PG8_CAT(*(const LAS i32x4*)(lds + PG8_SB(b, h) + boff + n * 2048), *(const LAS i32x4*)(lds + PG8_SB(b, h) + boff + n * 2048 + 1024)); } while (0)
; #define PG8_WAIT_V(n) asm volatile("s_waitcnt vmcnt(" #n ")" ::: "memory")
; #define PG8_WAIT_L(n) asm volatile("s_waitcnt lgkmcnt(" #n ")" ::: "memory")
; #define PG8_BAR __builtin_amdgcn_s_barrier()
; #define PG8_SCHED __builtin_amdgcn_sched_barrier(0)
; template <class Epi, class Sched>
; __device__ __forceinline__ void gemm_phase(LAS unsigned char* lds, const Sched& S, const Epi& E) {
;     ...
;         for (int t = 0; t < nt; t += 2) {
;             const bool last = (t == nt - 2);
;             const char* a1 = cA + PG8_KT(crot, t + 1);
;             const char* a2 = last ? nA + PG8_KT(nrot, 0) : cA + PG8_KT(crot, t + 2); const char* b2 = last ? nB + PG8_KT(nrot, 0) : cB + PG8_KT(crot, t + 2);
;             const char* a3 = last ? nA + PG8_KT(nrot, 1) : cA + PG8_KT(crot, t + 3); const char* b3 = last ? nB + PG8_KT(nrot, 1) : cB + PG8_KT(crot, t + 3);
;             int gi = 0;
;             if constexpr (Sched::GATHER) { if (t == 0 && has_next && tid < 256) gi = nxt.aidx[tid]; }
;             PG8_LDB(B0, 0, 0); PG8_LDB(B1, 0, 1); PG8_SCHED; PG8_LDA(At, 0, 0); PG8_STAGE(PG8_SA(1, 1), a1, vA[1]);
;             PG8_WAIT_V(8); PG8_WAIT_L(0); PG8_BAR; PG8_MMA(0, 0, At, B0); PG8_MMA(0, 1, At, B1); PG8_BAR2; PG8_SCHED;
.LBB0_210:
	s_add_i32 s17, s16, s91
	s_and_b32 s17, s17, 31
	s_and_b64 s[34:35], s[20:21], exec
	s_cselect_b32 s25, s17, s30
	s_lshl_b32 s31, s25, 7
	s_add_u32 s25, s18, s31
	s_addc_u32 s39, s19, 0
	s_add_u32 s40, s22, s31
	s_addc_u32 s41, s23, 0
	s_addk_i32 s31, 0x80
	s_and_b32 s31, s31, 0xf80
	s_add_u32 s44, s18, s31
	s_addc_u32 s45, s19, 0
	s_add_u32 s48, s22, s31
	s_addc_u32 s49, s23, 0
	s_lshl_b32 s30, s30, 7
	s_add_i32 s52, s30, 0x180
	s_mov_b32 s53, -2
	v_readfirstlane_b32 s100, v0
	s_bfe_u32 s100, s100, 0x20006
	s_cmp_gt_i32 s90, 14
	s_cselect_b32 s101, 1, 0
	s_cmp_lg_u32 s100, 0
	s_cselect_b32 s100, s101, 0
	s_add_i32 s30, s52, 0xffffff00
	s_add_i32 s31, s52, 0xffffff80
	s_and_b32 s30, s30, 0xf80
	s_and_b32 s31, s31, 0xf80
	s_add_u32 s34, s26, s31
	s_addc_u32 s35, s27, 0
	s_add_u32 s54, s28, s31
	s_addc_u32 s55, s29, 0
	s_and_b32 s31, s52, 0xf80
	s_add_u32 s92, s26, s31
	s_addc_u32 s93, s27, 0
	ds_read_b128 v[144:147], v140
	ds_read_b128 v[148:151], v140 offset:1024
	ds_read_b128 v[152:155], v140 offset:2048
	ds_read_b128 v[156:159], v140 offset:3072
	ds_read_b128 v[160:163], v141
	ds_read_b128 v[164:167], v141 offset:1024
	ds_read_b128 v[168:171], v141 offset:2048
	ds_read_b128 v[172:175], v141 offset:3072
	s_add_u32 s94, s28, s31
	s_addc_u32 s95, s29, 0
	s_add_u32 s36, s26, s30
	s_addc_u32 s37, s27, 0
	s_add_i32 vcc_lo, s75, s47
	s_add_i32 m0, s50, 0xc000
	s_add_i32 s97, s50, 0xe000
	s_add_i32 vcc_hi, vcc_lo, 0x2000
	s_cmp_eq_u32 s53, 28
	s_cselect_b32 s35, s39, s35
	s_cselect_b32 s34, s25, s34
	s_cselect_b32 s31, s45, s93
	s_cselect_b32 s30, s44, s92
	s_cselect_b32 s55, s41, s55
	s_cselect_b32 s54, s40, s54
	v_mov_b32_e32 v130, v137
	ds_read_b128 v[176:179], v142
	ds_read_b128 v[180:183], v142 offset:1024
	ds_read_b128 v[184:187], v142 offset:2048
	ds_read_b128 v[188:191], v142 offset:3072
	ds_read_b128 v[192:195], v142 offset:4096
	ds_read_b128 v[196:199], v142 offset:5120
	ds_read_b128 v[200:203], v142 offset:6144
	ds_read_b128 v[204:207], v142 offset:7168
	s_nop 0
	global_load_lds_dwordx4 v130, s[36:37]
	v_mov_b32_e32 v130, v138
	s_mov_b32 m0, s97
	s_nop 0
	global_load_lds_dwordx4 v130, s[36:37]
	s_waitcnt vmcnt(8)
	s_waitcnt lgkmcnt(0)
	s_barrier
	s_setprio 1
	s_waitcnt lgkmcnt(0)
	s_cmp_lg_u32 s100, 0
	s_cbranch_scc1 .Lpn15_skip1
	v_mfma_f32_16x16x32_bf16 v[126:129], v[144:147], v[176:179], 0
	v_mfma_f32_16x16x32_bf16 v[122:125], v[152:155], v[176:179], 0
	v_mfma_f32_16x16x32_bf16 v[118:121], v[144:147], v[184:187], 0
	v_mfma_f32_16x16x32_bf16 v[114:117], v[152:155], v[184:187], 0
	v_mfma_f32_16x16x32_bf16 v[102:105], v[144:147], v[192:195], 0
	v_mfma_f32_16x16x32_bf16 v[98:101], v[152:155], v[192:195], 0
	v_mfma_f32_16x16x32_bf16 v[86:89], v[144:147], v[200:203], 0
	v_mfma_f32_16x16x32_bf16 v[82:85], v[152:155], v[200:203], 0
	v_mfma_f32_16x16x32_bf16 v[126:129], v[148:151], v[180:183], v[126:129]
	v_mfma_f32_16x16x32_bf16 v[122:125], v[156:159], v[180:183], v[122:125]
	v_mfma_f32_16x16x32_bf16 v[118:121], v[148:151], v[188:191], v[118:121]
	v_mfma_f32_16x16x32_bf16 v[114:117], v[156:159], v[188:191], v[114:117]
	v_mfma_f32_16x16x32_bf16 v[102:105], v[148:151], v[196:199], v[102:105]
	v_mfma_f32_16x16x32_bf16 v[98:101], v[156:159], v[196:199], v[98:101]
	v_mfma_f32_16x16x32_bf16 v[86:89], v[148:151], v[204:207], v[86:89]
	v_mfma_f32_16x16x32_bf16 v[82:85], v[156:159], v[204:207], v[82:85]
	s_setprio 0
	s_setprio 1
	s_cmp_lg_u32 s101, 0
	s_cbranch_scc1 .Lpn15_skip1
	v_mfma_f32_16x16x32_bf16 v[110:113], v[160:163], v[176:179], 0
	v_mfma_f32_16x16x32_bf16 v[106:109], v[168:171], v[176:179], 0
	v_mfma_f32_16x16x32_bf16 v[94:97], v[160:163], v[184:187], 0
	v_mfma_f32_16x16x32_bf16 v[90:93], v[168:171], v[184:187], 0
	v_mfma_f32_16x16x32_bf16 v[78:81], v[160:163], v[192:195], 0
	v_mfma_f32_16x16x32_bf16 v[74:77], v[168:171], v[192:195], 0
	v_mfma_f32_16x16x32_bf16 v[70:73], v[160:163], v[200:203], 0
	v_mfma_f32_16x16x32_bf16 v[66:69], v[168:171], v[200:203], 0
	v_mfma_f32_16x16x32_bf16 v[110:113], v[164:167], v[180:183], v[110:113]
	v_mfma_f32_16x16x32_bf16 v[106:109], v[172:175], v[180:183], v[106:109]
	v_mfma_f32_16x16x32_bf16 v[94:97], v[164:167], v[188:191], v[94:97]
	v_mfma_f32_16x16x32_bf16 v[90:93], v[172:175], v[188:191], v[90:93]
	v_mfma_f32_16x16x32_bf16 v[78:81], v[164:167], v[196:199], v[78:81]
	v_mfma_f32_16x16x32_bf16 v[74:77], v[172:175], v[196:199], v[74:77]
	v_mfma_f32_16x16x32_bf16 v[70:73], v[164:167], v[204:207], v[70:73]
	v_mfma_f32_16x16x32_bf16 v[66:69], v[172:175], v[204:207], v[66:69]
; #define PG8_STAGE(bufoff, gbase, voff) do { if constexpr (!(Sched::CRIP & 2)) _Pragma("unroll") for (int _i = 0; _i < 2; ++_i) { unsigned _o = (voff)[_i]; asm volatile("" : "+v"(_o)); \
;         __builtin_amdgcn_global_load_lds((const unsigned*)((const char*)(gbase) + _o), (LAS unsigned*)(lds + (bufoff) + ldsw + _i * 8192), 16, 0, 0); } } while (0)
; #define PG8_LDA(dst, b, h) do { if constexpr (!(Sched::CRIP & 4)) _Pragma("unroll") for (int m = 0; m < 4; ++m) dst[m] = PG8_CAT(*(const LAS i32x4*)(lds + PG8_SA(b, h) + aoff + m * 2048), *(const LAS i32x4*)(lds + PG8_SA(b, h) + aoff + m * 2048 + 1024)); } while (0)
; #define PG8_LDB(dst, b, h) do { if constexpr (!(Sched::CRIP & 4)) _Pragma("unroll") for (int n = 0; n < 2; ++n) dst[n] = PG8_CAT(*(const LAS i32x4*)(lds + PG8_SB(b, h) + boff + n * 2048), *(const LAS i32x4*)(lds + PG8_SB(b, h) + boff + n * 2048 + 1024)); } while (0)
; #define PG8_WAIT_V(n) asm volatile("s_waitcnt vmcnt(" #n ")" ::: "memory")
; #define PG8_WAIT_L(n) asm volatile("s_waitcnt lgkmcnt(" #n ")" ::: "memory")
; #define PG8_BAR __builtin_amdgcn_s_barrier()
; #define PG8_SCHED __builtin_amdgcn_sched_barrier(0)
; template <class Epi, class Sched>
; __device__ __forceinline__ void gemm_phase(LAS unsigned char* lds, const Sched& S, const Epi& E) {
;     ...
;             PG8_LDA(At, 0, 1); PG8_STAGE(PG8_SB(0, 0), b2, voffB); PG8_STAGE(PG8_SB(0, 1), b2 + hstep, voffB); PG8_STAGE(PG8_SA(0, 0), a2, vA[0]);
;             PG8_WAIT_V(8); PG8_WAIT_L(0); PG8_BAR; PG8_MMA(1, 0, At, B0); PG8_MMA(1, 1, At, B1); PG8_BAR2; PG8_SCHED;
;             PG8_LDB(B0, 1, 0); PG8_LDB(B1, 1, 1); PG8_SCHED; PG8_LDA(At, 1, 0); PG8_STAGE(PG8_SA(0, 1), a2, vA[1]);
;             PG8_WAIT_V(8); PG8_WAIT_L(0); PG8_BAR; PG8_MMA(0, 0, At, B0); PG8_MMA(0, 1, At, B1); PG8_BAR2; PG8_SCHED;
.Lpn15_skip1:
	s_cmp_eq_u32 s53, 28
	s_setprio 0
	s_barrier
	v_mov_b32_e32 v130, v1
	s_mov_b32 m0, vcc_lo
	ds_read_b128 v[176:179], v142 offset:16384
	ds_read_b128 v[180:183], v142 offset:17408
	ds_read_b128 v[184:187], v142 offset:18432
	ds_read_b128 v[188:191], v142 offset:19456
	ds_read_b128 v[192:195], v142 offset:20480
	ds_read_b128 v[196:199], v142 offset:21504
	ds_read_b128 v[200:203], v142 offset:22528
	ds_read_b128 v[204:207], v142 offset:23552
	s_cselect_b32 s36, s48, s94
	global_load_lds_dwordx4 v130, s[54:55]
	v_mov_b32_e32 v130, v134
	s_mov_b32 m0, vcc_hi
	s_cselect_b32 s37, s49, s95
	global_load_lds_dwordx4 v130, s[54:55]
	s_add_u32 s54, s54, 0x80000
	v_mov_b32_e32 v130, v1
	s_addc_u32 s55, s55, 0
	s_add_i32 s92, s76, s47
	s_mov_b32 m0, s92
	s_nop 0
	global_load_lds_dwordx4 v130, s[54:55]
	v_mov_b32_e32 v130, v134
	s_add_i32 m0, s92, 0x2000
	s_nop 0
	global_load_lds_dwordx4 v130, s[54:55]
	v_mov_b32_e32 v130, v135
	s_mov_b32 m0, s50
	s_nop 0
	global_load_lds_dwordx4 v130, s[34:35]
	v_mov_b32_e32 v130, v136
	s_mov_b32 m0, s51
	s_nop 0
	global_load_lds_dwordx4 v130, s[34:35]
	s_waitcnt vmcnt(8)
	s_waitcnt lgkmcnt(0)
	s_barrier
	s_setprio 1
	s_waitcnt lgkmcnt(0)
	s_cmp_lg_u32 s100, 0
	s_cbranch_scc1 .Lpn15_skip2
	v_mfma_f32_16x16x32_bf16 v[62:65], v[144:147], v[176:179], 0
	v_mfma_f32_16x16x32_bf16 v[58:61], v[152:155], v[176:179], 0
	v_mfma_f32_16x16x32_bf16 v[54:57], v[144:147], v[184:187], 0
	v_mfma_f32_16x16x32_bf16 v[50:53], v[152:155], v[184:187], 0
	v_mfma_f32_16x16x32_bf16 v[38:41], v[144:147], v[192:195], 0
	v_mfma_f32_16x16x32_bf16 v[34:37], v[152:155], v[192:195], 0
	v_mfma_f32_16x16x32_bf16 v[22:25], v[144:147], v[200:203], 0
	v_mfma_f32_16x16x32_bf16 v[18:21], v[152:155], v[200:203], 0
	v_mfma_f32_16x16x32_bf16 v[62:65], v[148:151], v[180:183], v[62:65]
	v_mfma_f32_16x16x32_bf16 v[58:61], v[156:159], v[180:183], v[58:61]
	v_mfma_f32_16x16x32_bf16 v[54:57], v[148:151], v[188:191], v[54:57]
	v_mfma_f32_16x16x32_bf16 v[50:53], v[156:159], v[188:191], v[50:53]
	v_mfma_f32_16x16x32_bf16 v[38:41], v[148:151], v[196:199], v[38:41]
	v_mfma_f32_16x16x32_bf16 v[34:37], v[156:159], v[196:199], v[34:37]
	v_mfma_f32_16x16x32_bf16 v[22:25], v[148:151], v[204:207], v[22:25]
	v_mfma_f32_16x16x32_bf16 v[18:21], v[156:159], v[204:207], v[18:21]
	s_setprio 0
	s_setprio 1
	s_cmp_lg_u32 s101, 0
	s_cbranch_scc1 .Lpn15_skip2
	v_mfma_f32_16x16x32_bf16 v[46:49], v[160:163], v[176:179], 0
	v_mfma_f32_16x16x32_bf16 v[42:45], v[168:171], v[176:179], 0
	v_mfma_f32_16x16x32_bf16 v[30:33], v[160:163], v[184:187], 0
	v_mfma_f32_16x16x32_bf16 v[26:29], v[168:171], v[184:187], 0
	v_mfma_f32_16x16x32_bf16 v[14:17], v[160:163], v[192:195], 0
	v_mfma_f32_16x16x32_bf16 v[10:13], v[168:171], v[192:195], 0
	v_mfma_f32_16x16x32_bf16 v[6:9], v[160:163], v[200:203], 0
	v_mfma_f32_16x16x32_bf16 v[2:5], v[168:171], v[200:203], 0
	v_mfma_f32_16x16x32_bf16 v[46:49], v[164:167], v[180:183], v[46:49]
	v_mfma_f32_16x16x32_bf16 v[42:45], v[172:175], v[180:183], v[42:45]
	v_mfma_f32_16x16x32_bf16 v[30:33], v[164:167], v[188:191], v[30:33]
	v_mfma_f32_16x16x32_bf16 v[26:29], v[172:175], v[188:191], v[26:29]
	v_mfma_f32_16x16x32_bf16 v[14:17], v[164:167], v[196:199], v[14:17]
	v_mfma_f32_16x16x32_bf16 v[10:13], v[172:175], v[196:199], v[10:13]
	v_mfma_f32_16x16x32_bf16 v[6:9], v[164:167], v[204:207], v[6:9]
	v_mfma_f32_16x16x32_bf16 v[2:5], v[172:175], v[204:207], v[2:5]
.Lpn15_skip2:
	s_cmp_eq_u32 s53, 28
	s_setprio 0
	s_barrier
	s_add_i32 s54, 0, 0x18000
	v_add_u32_e32 v130, s54, v139
	s_add_i32 s55, 0, 0x1c000
	ds_read_b128 v[144:147], v130
	ds_read_b128 v[148:151], v130 offset:1024
	ds_read_b128 v[152:155], v130 offset:2048
	ds_read_b128 v[156:159], v130 offset:3072
	v_add_u32_e32 v130, s55, v139
	ds_read_b128 v[160:163], v130
	ds_read_b128 v[164:167], v130 offset:1024
	ds_read_b128 v[168:171], v130 offset:2048
	ds_read_b128 v[172:175], v130 offset:3072
	v_mov_b32_e32 v130, v137
	s_mov_b32 m0, s66
	ds_read_b128 v[176:179], v142 offset:32768
	ds_read_b128 v[180:183], v142 offset:33792
	ds_read_b128 v[184:187], v142 offset:34816
	ds_read_b128 v[188:191], v142 offset:35840
	ds_read_b128 v[192:195], v142 offset:36864
	ds_read_b128 v[196:199], v142 offset:37888
	ds_read_b128 v[200:203], v142 offset:38912
	ds_read_b128 v[204:207], v142 offset:39936
	s_nop 0
	global_load_lds_dwordx4 v130, s[34:35]
	v_mov_b32_e32 v130, v138
	s_mov_b32 m0, s67
	s_nop 0
	global_load_lds_dwordx4 v130, s[34:35]
	s_waitcnt vmcnt(8)
	s_waitcnt lgkmcnt(0)
	s_barrier
	s_setprio 1
	s_waitcnt lgkmcnt(0)
	s_cmp_lg_u32 s100, 0
	s_cbranch_scc1 .Lpn15_skip3
	v_mfma_f32_16x16x32_bf16 v[126:129], v[144:147], v[176:179], v[126:129]
	v_mfma_f32_16x16x32_bf16 v[122:125], v[152:155], v[176:179], v[122:125]
	v_mfma_f32_16x16x32_bf16 v[118:121], v[144:147], v[184:187], v[118:121]
	v_mfma_f32_16x16x32_bf16 v[114:117], v[152:155], v[184:187], v[114:117]
	v_mfma_f32_16x16x32_bf16 v[102:105], v[144:147], v[192:195], v[102:105]
	v_mfma_f32_16x16x32_bf16 v[98:101], v[152:155], v[192:195], v[98:101]
	v_mfma_f32_16x16x32_bf16 v[86:89], v[144:147], v[200:203], v[86:89]
	v_mfma_f32_16x16x32_bf16 v[82:85], v[152:155], v[200:203], v[82:85]
	v_mfma_f32_16x16x32_bf16 v[126:129], v[148:151], v[180:183], v[126:129]
	v_mfma_f32_16x16x32_bf16 v[122:125], v[156:159], v[180:183], v[122:125]
	v_mfma_f32_16x16x32_bf16 v[118:121], v[148:151], v[188:191], v[118:121]
	v_mfma_f32_16x16x32_bf16 v[114:117], v[156:159], v[188:191], v[114:117]
	v_mfma_f32_16x16x32_bf16 v[102:105], v[148:151], v[196:199], v[102:105]
	v_mfma_f32_16x16x32_bf16 v[98:101], v[156:159], v[196:199], v[98:101]
	v_mfma_f32_16x16x32_bf16 v[86:89], v[148:151], v[204:207], v[86:89]
	v_mfma_f32_16x16x32_bf16 v[82:85], v[156:159], v[204:207], v[82:85]
	s_setprio 0
	s_setprio 1
	s_cmp_lg_u32 s101, 0
	s_cbranch_scc1 .Lpn15_skip3
	v_mfma_f32_16x16x32_bf16 v[110:113], v[160:163], v[176:179], v[110:113]
	v_mfma_f32_16x16x32_bf16 v[106:109], v[168:171], v[176:179], v[106:109]
	v_mfma_f32_16x16x32_bf16 v[94:97], v[160:163], v[184:187], v[94:97]
	v_mfma_f32_16x16x32_bf16 v[90:93], v[168:171], v[184:187], v[90:93]
	v_mfma_f32_16x16x32_bf16 v[78:81], v[160:163], v[192:195], v[78:81]
	v_mfma_f32_16x16x32_bf16 v[74:77], v[168:171], v[192:195], v[74:77]
	v_mfma_f32_16x16x32_bf16 v[70:73], v[160:163], v[200:203], v[70:73]
	v_mfma_f32_16x16x32_bf16 v[66:69], v[168:171], v[200:203], v[66:69]
	v_mfma_f32_16x16x32_bf16 v[110:113], v[164:167], v[180:183], v[110:113]
	v_mfma_f32_16x16x32_bf16 v[106:109], v[172:175], v[180:183], v[106:109]
	v_mfma_f32_16x16x32_bf16 v[94:97], v[164:167], v[188:191], v[94:97]
	v_mfma_f32_16x16x32_bf16 v[90:93], v[172:175], v[188:191], v[90:93]
	v_mfma_f32_16x16x32_bf16 v[78:81], v[164:167], v[196:199], v[78:81]
	v_mfma_f32_16x16x32_bf16 v[74:77], v[172:175], v[196:199], v[74:77]
	v_mfma_f32_16x16x32_bf16 v[70:73], v[164:167], v[204:207], v[70:73]
	v_mfma_f32_16x16x32_bf16 v[66:69], v[172:175], v[204:207], v[66:69]
; #define PG8_STAGE(bufoff, gbase, voff) do { if constexpr (!(Sched::CRIP & 2)) _Pragma("unroll") for (int _i = 0; _i < 2; ++_i) { unsigned _o = (voff)[_i]; asm volatile("" : "+v"(_o)); \
;         __builtin_amdgcn_global_load_lds((const unsigned*)((const char*)(gbase) + _o), (LAS unsigned*)(lds + (bufoff) + ldsw + _i * 8192), 16, 0, 0); } } while (0)
; #define PG8_LDA(dst, b, h) do { if constexpr (!(Sched::CRIP & 4)) _Pragma("unroll") for (int m = 0; m < 4; ++m) dst[m] = PG8_CAT(*(const LAS i32x4*)(lds + PG8_SA(b, h) + aoff + m * 2048), *(const LAS i32x4*)(lds + PG8_SA(b, h) + aoff + m * 2048 + 1024)); } while (0)
; #define PG8_LDB(dst, b, h) do { if constexpr (!(Sched::CRIP & 4)) _Pragma("unroll") for (int n = 0; n < 2; ++n) dst[n] = PG8_CAT(*(const LAS i32x4*)(lds + PG8_SB(b, h) + boff + n * 2048), *(const LAS i32x4*)(lds + PG8_SB(b, h) + boff + n * 2048 + 1024)); } while (0)
; #define PG8_WAIT_V(n) asm volatile("s_waitcnt vmcnt(" #n ")" ::: "memory")
; #define PG8_WAIT_L(n) asm volatile("s_waitcnt lgkmcnt(" #n ")" ::: "memory")
; #define PG8_BAR __builtin_amdgcn_s_barrier()
; #define PG8_SCHED __builtin_amdgcn_sched_barrier(0)
; template <class Epi, class Sched>
; __device__ __forceinline__ void gemm_phase(LAS unsigned char* lds, const Sched& S, const Epi& E) {
;     ...
;         for (int t = 0; t < nt; t += 2) {
;             const bool last = (t == nt - 2);
;             const char* a1 = cA + PG8_KT(crot, t + 1);
;             const char* a2 = last ? nA + PG8_KT(nrot, 0) : cA + PG8_KT(crot, t + 2); const char* b2 = last ? nB + PG8_KT(nrot, 0) : cB + PG8_KT(crot, t + 2);
;             const char* a3 = last ? nA + PG8_KT(nrot, 1) : cA + PG8_KT(crot, t + 3); const char* b3 = last ? nB + PG8_KT(nrot, 1) : cB + PG8_KT(crot, t + 3);
;             int gi = 0;
;             if constexpr (Sched::GATHER) { if (t == 0 && has_next && tid < 256) gi = nxt.aidx[tid]; }
;             PG8_LDB(B0, 0, 0); PG8_LDB(B1, 0, 1); PG8_SCHED; PG8_LDA(At, 0, 0); PG8_STAGE(PG8_SA(1, 1), a1, vA[1]);
;             PG8_WAIT_V(8); PG8_WAIT_L(0); PG8_BAR; PG8_MMA(0, 0, At, B0); PG8_MMA(0, 1, At, B1); PG8_BAR2; PG8_SCHED;
;     ...
;             PG8_LDA(At, 1, 1); PG8_STAGE(PG8_SB(1, 0), b3, voffB); PG8_STAGE(PG8_SB(1, 1), b3 + hstep, voffB); PG8_STAGE(PG8_SA(1, 0), a3, vA[0]);
;             PG8_WAIT_V(8); PG8_WAIT_L(0); PG8_BAR; PG8_MMA(1, 0, At, B0); PG8_MMA(1, 1, At, B1); PG8_BAR2; PG8_SCHED;
.Lpn15_skip3:
	s_cmp_eq_u32 s53, 28
	s_setprio 0
	s_barrier
	v_mov_b32_e32 v130, v1
	s_add_i32 s34, s54, s47
	ds_read_b128 v[176:179], v142 offset:49152
	ds_read_b128 v[180:183], v142 offset:50176
	ds_read_b128 v[184:187], v142 offset:51200
	ds_read_b128 v[188:191], v142 offset:52224
	ds_read_b128 v[192:195], v142 offset:53248
	ds_read_b128 v[196:199], v142 offset:54272
	ds_read_b128 v[200:203], v142 offset:55296
	ds_read_b128 v[204:207], v142 offset:56320
	s_mov_b32 m0, s34
	s_nop 0
	global_load_lds_dwordx4 v130, s[36:37]
	v_mov_b32_e32 v130, v134
	s_add_i32 m0, s34, 0x2000
	s_add_u32 s34, s36, 0x80000
	global_load_lds_dwordx4 v130, s[36:37]
	s_addc_u32 s35, s37, 0
	v_mov_b32_e32 v130, v1
	s_add_i32 s36, s55, s47
	s_mov_b32 m0, s36
	s_nop 0
	global_load_lds_dwordx4 v130, s[34:35]
	v_mov_b32_e32 v130, v134
	s_add_i32 m0, s36, 0x2000
	s_nop 0
	global_load_lds_dwordx4 v130, s[34:35]
	v_mov_b32_e32 v130, v135
	s_mov_b32 m0, s70
	s_nop 0
	global_load_lds_dwordx4 v130, s[30:31]
	v_mov_b32_e32 v130, v136
	s_mov_b32 m0, s71
	s_nop 0
	global_load_lds_dwordx4 v130, s[30:31]
	s_waitcnt vmcnt(8)
	s_waitcnt lgkmcnt(0)
	s_barrier
	s_setprio 1
	s_waitcnt lgkmcnt(0)
	s_cmp_lg_u32 s100, 0
	s_cbranch_scc1 .Lpn15_skip4
	v_mfma_f32_16x16x32_bf16 v[62:65], v[144:147], v[176:179], v[62:65]
	v_mfma_f32_16x16x32_bf16 v[58:61], v[152:155], v[176:179], v[58:61]
	v_mfma_f32_16x16x32_bf16 v[54:57], v[144:147], v[184:187], v[54:57]
	v_mfma_f32_16x16x32_bf16 v[50:53], v[152:155], v[184:187], v[50:53]
	v_mfma_f32_16x16x32_bf16 v[38:41], v[144:147], v[192:195], v[38:41]
	v_mfma_f32_16x16x32_bf16 v[34:37], v[152:155], v[192:195], v[34:37]
	v_mfma_f32_16x16x32_bf16 v[22:25], v[144:147], v[200:203], v[22:25]
	v_mfma_f32_16x16x32_bf16 v[18:21], v[152:155], v[200:203], v[18:21]
	v_mfma_f32_16x16x32_bf16 v[62:65], v[148:151], v[180:183], v[62:65]
	v_mfma_f32_16x16x32_bf16 v[58:61], v[156:159], v[180:183], v[58:61]
	v_mfma_f32_16x16x32_bf16 v[54:57], v[148:151], v[188:191], v[54:57]
	v_mfma_f32_16x16x32_bf16 v[50:53], v[156:159], v[188:191], v[50:53]
	v_mfma_f32_16x16x32_bf16 v[38:41], v[148:151], v[196:199], v[38:41]
	v_mfma_f32_16x16x32_bf16 v[34:37], v[156:159], v[196:199], v[34:37]
	v_mfma_f32_16x16x32_bf16 v[22:25], v[148:151], v[204:207], v[22:25]
	v_mfma_f32_16x16x32_bf16 v[18:21], v[156:159], v[204:207], v[18:21]
	s_setprio 0
	s_setprio 1
	s_cmp_lg_u32 s101, 0
	s_cbranch_scc1 .Lpn15_skip4
	v_mfma_f32_16x16x32_bf16 v[46:49], v[160:163], v[176:179], v[46:49]
	v_mfma_f32_16x16x32_bf16 v[42:45], v[168:171], v[176:179], v[42:45]
	v_mfma_f32_16x16x32_bf16 v[30:33], v[160:163], v[184:187], v[30:33]
	v_mfma_f32_16x16x32_bf16 v[26:29], v[168:171], v[184:187], v[26:29]
	v_mfma_f32_16x16x32_bf16 v[14:17], v[160:163], v[192:195], v[14:17]
	v_mfma_f32_16x16x32_bf16 v[10:13], v[168:171], v[192:195], v[10:13]
	v_mfma_f32_16x16x32_bf16 v[6:9], v[160:163], v[200:203], v[6:9]
	v_mfma_f32_16x16x32_bf16 v[2:5], v[168:171], v[200:203], v[2:5]
	v_mfma_f32_16x16x32_bf16 v[46:49], v[164:167], v[180:183], v[46:49]
	v_mfma_f32_16x16x32_bf16 v[42:45], v[172:175], v[180:183], v[42:45]
	v_mfma_f32_16x16x32_bf16 v[30:33], v[164:167], v[188:191], v[30:33]
	v_mfma_f32_16x16x32_bf16 v[26:29], v[172:175], v[188:191], v[26:29]
	v_mfma_f32_16x16x32_bf16 v[14:17], v[164:167], v[196:199], v[14:17]
	v_mfma_f32_16x16x32_bf16 v[10:13], v[172:175], v[196:199], v[10:13]
	v_mfma_f32_16x16x32_bf16 v[6:9], v[164:167], v[204:207], v[6:9]
	v_mfma_f32_16x16x32_bf16 v[2:5], v[172:175], v[204:207], v[2:5]
.Lpn15_skip4:
	s_cmp_eq_u32 s53, 28
	s_setprio 0
	s_barrier
	s_add_i32 s53, s53, 2
	s_addk_i32 s52, 0x100
.LBB0_211:
	s_add_i32 s30, s52, 0xffffff00
	s_add_i32 s31, s52, 0xffffff80
	s_and_b32 s30, s30, 0xf80
	s_and_b32 s31, s31, 0xf80
	s_add_u32 s34, s26, s31
	s_addc_u32 s35, s27, 0
	s_add_u32 s54, s28, s31
	s_addc_u32 s55, s29, 0
	s_and_b32 s31, s52, 0xf80
	s_add_u32 s92, s26, s31
	s_addc_u32 s93, s27, 0
	ds_read_b128 v[144:147], v140
	ds_read_b128 v[148:151], v140 offset:1024
	ds_read_b128 v[152:155], v140 offset:2048
	ds_read_b128 v[156:159], v140 offset:3072
	ds_read_b128 v[160:163], v141
	ds_read_b128 v[164:167], v141 offset:1024
	ds_read_b128 v[168:171], v141 offset:2048
	ds_read_b128 v[172:175], v141 offset:3072
	s_add_u32 s94, s28, s31
	s_addc_u32 s95, s29, 0
	s_add_u32 s36, s26, s30
	s_addc_u32 s37, s27, 0
	s_add_i32 vcc_lo, s75, s47
	s_add_i32 m0, s50, 0xc000
	s_add_i32 s97, s50, 0xe000
	s_add_i32 vcc_hi, vcc_lo, 0x2000
	s_cmp_eq_u32 s53, 28
	s_cselect_b32 s35, s39, s35
	s_cselect_b32 s34, s25, s34
	s_cselect_b32 s31, s45, s93
	s_cselect_b32 s30, s44, s92
	s_cselect_b32 s55, s41, s55
	s_cselect_b32 s54, s40, s54
	v_mov_b32_e32 v130, v137
	ds_read_b128 v[176:179], v142
	ds_read_b128 v[180:183], v142 offset:1024
	ds_read_b128 v[184:187], v142 offset:2048
	ds_read_b128 v[188:191], v142 offset:3072
	ds_read_b128 v[192:195], v142 offset:4096
	ds_read_b128 v[196:199], v142 offset:5120
	ds_read_b128 v[200:203], v142 offset:6144
	ds_read_b128 v[204:207], v142 offset:7168
	s_nop 0
	global_load_lds_dwordx4 v130, s[36:37]
	v_mov_b32_e32 v130, v138
	s_mov_b32 m0, s97
	s_nop 0
	global_load_lds_dwordx4 v130, s[36:37]
	s_waitcnt vmcnt(8)
	s_waitcnt lgkmcnt(0)
	s_barrier
	s_setprio 1
	s_waitcnt lgkmcnt(0)
	s_cmp_lg_u32 s100, 0
	s_cbranch_scc1 .Lpn15_skip5
; #define PG8_STAGE(bufoff, gbase, voff) do { if constexpr (!(Sched::CRIP & 2)) _Pragma("unroll") for (int _i = 0; _i < 2; ++_i) { unsigned _o = (voff)[_i]; asm volatile("" : "+v"(_o)); \
;         __builtin_amdgcn_global_load_lds((const unsigned*)((const char*)(gbase) + _o), (LAS unsigned*)(lds + (bufoff) + ldsw + _i * 8192), 16, 0, 0); } } while (0)
; #define PG8_LDA(dst, b, h) do { if constexpr (!(Sched::CRIP & 4)) _Pragma("unroll") for (int m = 0; m < 4; ++m) dst[m] = PG8_CAT(*(const LAS i32x4*)(lds + PG8_SA(b, h) + aoff + m * 2048), *(const LAS i32x4*)(lds + PG8_SA(b, h) + aoff + m * 2048 + 1024)); } while (0)
; #define PG8_LDB(dst, b, h) do { if constexpr (!(Sched::CRIP & 4)) _Pragma("unroll") for (int n = 0; n < 2; ++n) dst[n] = PG8_CAT(*(const LAS i32x4*)(lds + PG8_SB(b, h) + boff + n * 2048), *(const LAS i32x4*)(lds + PG8_SB(b, h) + boff + n * 2048 + 1024)); } while (0)
; #define PG8_WAIT_V(n) asm volatile("s_waitcnt vmcnt(" #n ")" ::: "memory")
; #define PG8_WAIT_L(n) asm volatile("s_waitcnt lgkmcnt(" #n ")" ::: "memory")
; #define PG8_BAR __builtin_amdgcn_s_barrier()
; #define PG8_SCHED __builtin_amdgcn_sched_barrier(0)
; template <class Epi, class Sched>
; __device__ __forceinline__ void gemm_phase(LAS unsigned char* lds, const Sched& S, const Epi& E) {
;     ...
;             PG8_WAIT_V(8); PG8_WAIT_L(0); PG8_BAR; PG8_MMA(0, 0, At, B0); PG8_MMA(0, 1, At, B1); PG8_BAR2; PG8_SCHED;
;             if constexpr (Sched::GATHER) { if (last && has_next) {
;                 int tz = threadIdx.x; asm volatile("" : "+v"(tz));
; #pragma unroll
;                 for (int i = 0; i < 2; ++i) { int R, C; stage_rc(tz * 16 + i * 8192, R, C);
; #pragma unroll
;                     for (int h = 0; h < 2; ++h) vA[h][i] = (unsigned)(lidx[h * HALF + R] * RP + C * 2); } } }
;             PG8_LDA(At, 0, 1); PG8_STAGE(PG8_SB(0, 0), b2, voffB); PG8_STAGE(PG8_SB(0, 1), b2 + hstep, voffB); PG8_STAGE(PG8_SA(0, 0), a2, vA[0]);
;             PG8_WAIT_V(8); PG8_WAIT_L(0); PG8_BAR; PG8_MMA(1, 0, At, B0); PG8_MMA(1, 1, At, B1); PG8_BAR2; PG8_SCHED;
;             PG8_LDB(B0, 1, 0); PG8_LDB(B1, 1, 1); PG8_SCHED; PG8_LDA(At, 1, 0); PG8_STAGE(PG8_SA(0, 1), a2, vA[1]);
;             PG8_WAIT_V(8); PG8_WAIT_L(0); PG8_BAR; PG8_MMA(0, 0, At, B0); PG8_MMA(0, 1, At, B1); PG8_BAR2; PG8_SCHED;
	v_mfma_f32_16x16x32_bf16 v[126:129], v[144:147], v[176:179], v[126:129]
	v_mfma_f32_16x16x32_bf16 v[122:125], v[152:155], v[176:179], v[122:125]
	v_mfma_f32_16x16x32_bf16 v[118:121], v[144:147], v[184:187], v[118:121]
	v_mfma_f32_16x16x32_bf16 v[114:117], v[152:155], v[184:187], v[114:117]
	v_mfma_f32_16x16x32_bf16 v[102:105], v[144:147], v[192:195], v[102:105]
	v_mfma_f32_16x16x32_bf16 v[98:101], v[152:155], v[192:195], v[98:101]
	v_mfma_f32_16x16x32_bf16 v[86:89], v[144:147], v[200:203], v[86:89]
	v_mfma_f32_16x16x32_bf16 v[82:85], v[152:155], v[200:203], v[82:85]
	v_mfma_f32_16x16x32_bf16 v[126:129], v[148:151], v[180:183], v[126:129]
	v_mfma_f32_16x16x32_bf16 v[122:125], v[156:159], v[180:183], v[122:125]
	v_mfma_f32_16x16x32_bf16 v[118:121], v[148:151], v[188:191], v[118:121]
	v_mfma_f32_16x16x32_bf16 v[114:117], v[156:159], v[188:191], v[114:117]
	v_mfma_f32_16x16x32_bf16 v[102:105], v[148:151], v[196:199], v[102:105]
	v_mfma_f32_16x16x32_bf16 v[98:101], v[156:159], v[196:199], v[98:101]
	v_mfma_f32_16x16x32_bf16 v[86:89], v[148:151], v[204:207], v[86:89]
	v_mfma_f32_16x16x32_bf16 v[82:85], v[156:159], v[204:207], v[82:85]
	s_setprio 0
	s_setprio 1
	s_cmp_lg_u32 s101, 0
	s_cbranch_scc1 .Lpn15_skip5
	v_mfma_f32_16x16x32_bf16 v[110:113], v[160:163], v[176:179], v[110:113]
	v_mfma_f32_16x16x32_bf16 v[106:109], v[168:171], v[176:179], v[106:109]
	v_mfma_f32_16x16x32_bf16 v[94:97], v[160:163], v[184:187], v[94:97]
	v_mfma_f32_16x16x32_bf16 v[90:93], v[168:171], v[184:187], v[90:93]
	v_mfma_f32_16x16x32_bf16 v[78:81], v[160:163], v[192:195], v[78:81]
	v_mfma_f32_16x16x32_bf16 v[74:77], v[168:171], v[192:195], v[74:77]
	v_mfma_f32_16x16x32_bf16 v[70:73], v[160:163], v[200:203], v[70:73]
	v_mfma_f32_16x16x32_bf16 v[66:69], v[168:171], v[200:203], v[66:69]
	v_mfma_f32_16x16x32_bf16 v[110:113], v[164:167], v[180:183], v[110:113]
	v_mfma_f32_16x16x32_bf16 v[106:109], v[172:175], v[180:183], v[106:109]
	v_mfma_f32_16x16x32_bf16 v[94:97], v[164:167], v[188:191], v[94:97]
	v_mfma_f32_16x16x32_bf16 v[90:93], v[172:175], v[188:191], v[90:93]
	v_mfma_f32_16x16x32_bf16 v[78:81], v[164:167], v[196:199], v[78:81]
	v_mfma_f32_16x16x32_bf16 v[74:77], v[172:175], v[196:199], v[74:77]
	v_mfma_f32_16x16x32_bf16 v[70:73], v[164:167], v[204:207], v[70:73]
	v_mfma_f32_16x16x32_bf16 v[66:69], v[172:175], v[204:207], v[66:69]
.Lpn15_skip5:
	s_cmp_eq_u32 s53, 28
	s_setprio 0
	s_barrier
	v_mov_b32_e32 v130, v1
	s_mov_b32 m0, vcc_lo
	ds_read_b128 v[176:179], v142 offset:16384
	ds_read_b128 v[180:183], v142 offset:17408
	ds_read_b128 v[184:187], v142 offset:18432
	ds_read_b128 v[188:191], v142 offset:19456
	ds_read_b128 v[192:195], v142 offset:20480
	ds_read_b128 v[196:199], v142 offset:21504
	ds_read_b128 v[200:203], v142 offset:22528
	ds_read_b128 v[204:207], v142 offset:23552
	s_cselect_b32 s36, s48, s94
	global_load_lds_dwordx4 v130, s[54:55]
	v_mov_b32_e32 v130, v134
	s_mov_b32 m0, vcc_hi
	s_cselect_b32 s37, s49, s95
	global_load_lds_dwordx4 v130, s[54:55]
	s_add_u32 s54, s54, 0x80000
	v_mov_b32_e32 v130, v1
	s_addc_u32 s55, s55, 0
	s_add_i32 s92, s76, s47
	s_mov_b32 m0, s92
	s_nop 0
	global_load_lds_dwordx4 v130, s[54:55]
	v_mov_b32_e32 v130, v134
	s_add_i32 m0, s92, 0x2000
	s_nop 0
	global_load_lds_dwordx4 v130, s[54:55]
	v_mov_b32_e32 v130, v135
	s_mov_b32 m0, s50
	s_nop 0
	global_load_lds_dwordx4 v130, s[34:35]
	v_mov_b32_e32 v130, v136
	s_mov_b32 m0, s51
	s_nop 0
	global_load_lds_dwordx4 v130, s[34:35]
	s_waitcnt vmcnt(8)
	s_waitcnt lgkmcnt(0)
	s_barrier
	s_setprio 1
	s_waitcnt lgkmcnt(0)
	s_cmp_lg_u32 s100, 0
	s_cbranch_scc1 .Lpn15_skip6
	v_mfma_f32_16x16x32_bf16 v[62:65], v[144:147], v[176:179], v[62:65]
	v_mfma_f32_16x16x32_bf16 v[58:61], v[152:155], v[176:179], v[58:61]
	v_mfma_f32_16x16x32_bf16 v[54:57], v[144:147], v[184:187], v[54:57]
	v_mfma_f32_16x16x32_bf16 v[50:53], v[152:155], v[184:187], v[50:53]
	v_mfma_f32_16x16x32_bf16 v[38:41], v[144:147], v[192:195], v[38:41]
	v_mfma_f32_16x16x32_bf16 v[34:37], v[152:155], v[192:195], v[34:37]
	v_mfma_f32_16x16x32_bf16 v[22:25], v[144:147], v[200:203], v[22:25]
	v_mfma_f32_16x16x32_bf16 v[18:21], v[152:155], v[200:203], v[18:21]
	v_mfma_f32_16x16x32_bf16 v[62:65], v[148:151], v[180:183], v[62:65]
	v_mfma_f32_16x16x32_bf16 v[58:61], v[156:159], v[180:183], v[58:61]
	v_mfma_f32_16x16x32_bf16 v[54:57], v[148:151], v[188:191], v[54:57]
	v_mfma_f32_16x16x32_bf16 v[50:53], v[156:159], v[188:191], v[50:53]
	v_mfma_f32_16x16x32_bf16 v[38:41], v[148:151], v[196:199], v[38:41]
	v_mfma_f32_16x16x32_bf16 v[34:37], v[156:159], v[196:199], v[34:37]
	v_mfma_f32_16x16x32_bf16 v[22:25], v[148:151], v[204:207], v[22:25]
	v_mfma_f32_16x16x32_bf16 v[18:21], v[156:159], v[204:207], v[18:21]
	s_setprio 0
	s_setprio 1
	s_cmp_lg_u32 s101, 0
	s_cbranch_scc1 .Lpn15_skip6
	v_mfma_f32_16x16x32_bf16 v[46:49], v[160:163], v[176:179], v[46:49]
	v_mfma_f32_16x16x32_bf16 v[42:45], v[168:171], v[176:179], v[42:45]
	v_mfma_f32_16x16x32_bf16 v[30:33], v[160:163], v[184:187], v[30:33]
	v_mfma_f32_16x16x32_bf16 v[26:29], v[168:171], v[184:187], v[26:29]
	v_mfma_f32_16x16x32_bf16 v[14:17], v[160:163], v[192:195], v[14:17]
	v_mfma_f32_16x16x32_bf16 v[10:13], v[168:171], v[192:195], v[10:13]
	v_mfma_f32_16x16x32_bf16 v[6:9], v[160:163], v[200:203], v[6:9]
	v_mfma_f32_16x16x32_bf16 v[2:5], v[168:171], v[200:203], v[2:5]
	v_mfma_f32_16x16x32_bf16 v[46:49], v[164:167], v[180:183], v[46:49]
	v_mfma_f32_16x16x32_bf16 v[42:45], v[172:175], v[180:183], v[42:45]
	v_mfma_f32_16x16x32_bf16 v[30:33], v[164:167], v[188:191], v[30:33]
	v_mfma_f32_16x16x32_bf16 v[26:29], v[172:175], v[188:191], v[26:29]
	v_mfma_f32_16x16x32_bf16 v[14:17], v[164:167], v[196:199], v[14:17]
	v_mfma_f32_16x16x32_bf16 v[10:13], v[172:175], v[196:199], v[10:13]
	v_mfma_f32_16x16x32_bf16 v[6:9], v[164:167], v[204:207], v[6:9]
	v_mfma_f32_16x16x32_bf16 v[2:5], v[172:175], v[204:207], v[2:5]

; #define PG8_WAIT_V(n) asm volatile("s_waitcnt vmcnt(" #n ")" ::: "memory")
; #define PG8_WAIT_L(n) asm volatile("s_waitcnt lgkmcnt(" #n ")" ::: "memory")
; #define PG8_BAR __builtin_amdgcn_s_barrier()
; #define PG8_SCHED __builtin_amdgcn_sched_barrier(0)
; template <class Epi, class Sched>
; __device__ __forceinline__ void gemm_phase(LAS unsigned char* lds, const Sched& S, const Epi& E) {
;     ...
;             PG8_WAIT_V(8); PG8_WAIT_L(0); PG8_BAR; PG8_MMA(1, 0, At, B0); PG8_MMA(1, 1, At, B1); PG8_BAR2; PG8_SCHED;
;             if constexpr (Sched::GATHER) { if (t == 0 && has_next && tid < 256) lidx[tid] = (tid < nxt.avalid) ? gi : 0; }
;         }
;     __device__ __forceinline__ bool next(int i, Unit& u) const {
;         const int t = __builtin_amdgcn_readfirstlane(tk[i & 1]);
;         if (i > 0 && threadIdx.x == 0) tk[(i + 1) & 1] = (int)__hip_atomic_fetch_add(tick, 1u, __ATOMIC_RELAXED, __HIP_MEMORY_SCOPE_AGENT);
.Lpn15_skip8:
	s_cmp_eq_u32 s53, 28
	s_setprio 0
	s_barrier
	s_add_i32 s53, s53, 2
	s_addk_i32 s52, 0x100
	s_cmp_gt_u32 s53, 29
	s_cbranch_scc0 .LBB0_211
	s_and_saveexec_b64 s[98:99], s[0:1]
	s_cbranch_execz .Ltk_done
	s_and_b32 s100, s74, 1
	s_xor_b32 s100, s100, 1
	s_lshl_b32 s100, s100, 2
	s_add_i32 s100, s100, 0x27f00
	s_waitcnt vmcnt(8)
	v_readfirstlane_b32 s101, v246
	v_mov_b32_e32 v248, s100
	s_nop 0
	v_add_u32_e32 v247, s101, v247
	ds_write_b32 v248, v247
	s_waitcnt lgkmcnt(0)
